# P3 GLA scan: output waves start MFMAs on counted lgkmcnt, two independent accumulation chains, early store addresses; state update split waves 0/7
# speedup vs baseline: 1.0046x; 1.0046x over previous
; #define LAS __attribute__((address_space(3)))
; __device__ __forceinline__ unsigned f2bf(float f) { unsigned u = __builtin_bit_cast(unsigned, f); return (u + 0x7fffu + ((u >> 16) & 1u)) >> 16; }
; __device__ __forceinline__ void gs_vfrag(const LAS unsigned char* vbase, int lane, bf16x8 (&vf)[2]) {
;     const unsigned a = (unsigned)(uintptr_t)(vbase + (8 * (lane >> 4) + ((lane & 15) >> 2)) * 32 + (lane & 3) * 8);
;     s16x4 r0, r1, r2, r3;
;     asm volatile("ds_read_b64_tr_b16 %0, %4\n\tds_read_b64_tr_b16 %1, %4 offset:128\n\tds_read_b64_tr_b16 %2, %4 offset:1024\n\tds_read_b64_tr_b16 %3, %4 offset:1152\n\ts_waitcnt lgkmcnt(0)"
;                  : "=&v"(r0), "=&v"(r1), "=&v"(r2), "=&v"(r3) : "v"(a) : "memory");
;     vf[0] = (bf16x8){r0[0], r0[1], r0[2], r0[3], r1[0], r1[1], r1[2], r1[3]}; vf[1] = (bf16x8){r2[0], r2[1], r2[2], r2[3], r3[0], r3[1], r3[2], r3[3]};
; }
; __device__ __forceinline__ void gla_scan_chain(Frame& F, int chain) {
;     ...
;         } else if (wave <= 4) {
;             const int m = wave - 1, r = 16 * m + fr;
;             bf16x8 vf[2]; gs_vfrag(base + GS_V, lane, vf);
;             const LAS unsigned char* sb = F.lds + GS_SB + (n & 1) * GS_SBBUF + fr * GS_SBROW + 16 * fq;
;             bf16x8 af[2], qf[4], sf[4];
; #pragma unroll
;             for (int ks = 0; ks < 2; ++ks) af[ks] = *(const LAS bf16x8*)(base + GS_AM + r * 128 + (((4 * ks + fq) ^ (r & 7)) * 16));
; #pragma unroll
;             for (int ks = 0; ks < 4; ++ks) { qf[ks] = *(const LAS bf16x8*)(base + GS_QIN + r * 256 + (((4 * ks + fq) ^ (r & 15)) * 16)); sf[ks] = *(const LAS bf16x8*)(sb + 64 * ks); }
;             __builtin_amdgcn_sched_barrier(0);
;             f32x4 acc = (f32x4){0.f, 0.f, 0.f, 0.f};
; #pragma unroll
;             for (int ks = 0; ks < 2; ++ks) acc = __builtin_amdgcn_mfma_f32_16x16x32_bf16(af[ks], vf[ks], acc, 0, 0, 0);
; #pragma unroll
;             for (int ks = 0; ks < 4; ++ks) acc = __builtin_amdgcn_mfma_f32_16x16x32_bf16(qf[ks], sf[ks], acc, 0, 0, 0);
;             bf16_t* op = ORAW + ((size_t)b * SEQ + 64 * n + 16 * m + 4 * fq) * 2048 + h * 256 + et * 16 + fr;
; #pragma unroll
;             for (int i = 0; i < 4; ++i) op[(size_t)i * 2048] = (bf16_t)f2bf(acc[i]);
;         }
.LBB0_375:
	s_andn2_b64 vcc, exec, s[10:11]
	s_cbranch_vccnz .Lgs_w567
	v_add_u32_e32 v3, s34, v92
	v_add3_u32 v3, v3, v93, s51
	ds_read_b64_tr_b16 v[112:113], v3
	ds_read_b64_tr_b16 v[114:115], v3 offset:128
	ds_read_b64_tr_b16 v[108:109], v3 offset:1024
	ds_read_b64_tr_b16 v[110:111], v3 offset:1152
	v_add_u32_e32 v3, s34, v95
	v_add_u32_e32 v4, v3, v98
	s_bitcmp1_b32 s37, 0
	v_add_u32_e32 v3, v3, v99
	ds_read_b128 v[116:119], v4
	ds_read_b128 v[120:123], v3
	v_add_u32_e32 v4, s34, v96
	s_cselect_b32 s30, 0x1100, 0
	v_add_u32_e32 v5, v4, v100
	v_add_u32_e32 v3, s30, v104
	v_add_u32_e32 v128, v4, v101
	ds_read_b128 v[124:127], v5 offset:8192
	ds_read_b128 v[136:139], v3
	ds_read_b128 v[132:135], v128 offset:8192
	ds_read_b128 v[140:143], v3 offset:64
	v_add_u32_e32 v5, v4, v102
	v_add_u32_e32 v4, v4, v103
	ds_read_b128 v[144:147], v5 offset:8192
	ds_read_b128 v[156:159], v3 offset:128
	ds_read_b128 v[148:151], v4 offset:8192
	ds_read_b128 v[160:163], v3 offset:192
	v_lshl_add_u64 v[164:165], v[90:91], 0, s[18:19]
	s_mov_b64 s[30:31], 0x61ff1000
	v_lshl_add_u64 v[166:167], v[164:165], 0, s[30:31]
	s_mov_b64 s[30:31], 0x61ff3000
	v_lshl_add_u64 v[164:165], v[164:165], 0, s[30:31]
	s_waitcnt lgkmcnt(9)
	v_mfma_f32_16x16x32_bf16 v[112:115], v[116:119], v[112:115], 0
	s_waitcnt lgkmcnt(6)
	v_mfma_f32_16x16x32_bf16 v[170:173], v[124:127], v[136:139], 0
	v_mfma_f32_16x16x32_bf16 v[108:111], v[120:123], v[108:111], v[112:115]
	s_waitcnt lgkmcnt(4)
	v_mfma_f32_16x16x32_bf16 v[170:173], v[132:135], v[140:143], v[170:173]
	s_waitcnt lgkmcnt(2)
	v_mfma_f32_16x16x32_bf16 v[170:173], v[144:147], v[156:159], v[170:173]
	s_waitcnt lgkmcnt(0)
	v_mfma_f32_16x16x32_bf16 v[170:173], v[148:151], v[160:163], v[170:173]
	s_nop 7
	s_nop 1
	v_pk_add_f32 v[108:109], v[108:109], v[170:171]
	v_pk_add_f32 v[110:111], v[110:111], v[172:173]
	s_nop 0
	v_cvt_pk_bf16_f32 v3, v108, v109
	v_cvt_pk_bf16_f32 v116, v110, v111
	global_store_short v[166:167], v3, off offset:-4096
	global_store_short_d16_hi v[166:167], v3, off
	global_store_short v[164:165], v116, off offset:-4096
	global_store_short_d16_hi v[164:165], v116, off
	s_branch .LBB0_377
